# G4(0) tail conversion slot enlarged to 24000 items (MODUL(1) keeps 38400)
# speedup vs baseline: 1.0002x; 1.0002x over previous
.LBB0_160:
	v_readlane_b32 s0, v251, 11
	v_readlane_b32 s1, v251, 12
	s_and_b64 s[0:1], s[0:1], s[2:3]
	s_andn2_b64 vcc, exec, s[0:1]
	s_cbranch_vccnz .LBB0_201
	v_readlane_b32 s0, v251, 13
	s_add_i32 s0, s25, s0
	s_cmp_gt_i32 s0, 0x95ff
	s_waitcnt lgkmcnt(0)
	s_barrier
	s_cbranch_scc1 .LBB0_201
	s_add_u32 s28, s14, 0x5800000
	s_addc_u32 s29, s15, 0
	s_add_u32 s30, s34, 0x19a00000
	s_mulk_i32 s25, 0x2200
	s_waitcnt vmcnt(0)
	v_and_b32_e32 v11, 7, v145
	s_addc_u32 s31, s35, 0
	s_add_i32 s2, s0, 0x6d60
	s_add_i32 s0, s25, 0
	v_lshrrev_b32_e32 v13, 3, v144
	v_lshlrev_b32_e32 v0, 4, v11
	v_add_u32_e32 v3, s0, v0
	s_waitcnt vmcnt(0)
	v_mul_u32_u24_e32 v7, 0x420, v11
	v_lshl_add_u64 v[22:23], s[14:15], 0, v[0:1]
	v_lshlrev_b32_e32 v0, 2, v13
	v_add3_u32 v7, s0, v7, v0
	s_movk_i32 s0, 0xb00
	v_mov_b32_e32 v0, 0x16000
	v_mad_u32_u24 v46, v13, s0, v0
	v_mov_b32_e32 v0, 0x1b800
	v_mad_u32_u24 v48, v13, s0, v0
	v_mov_b32_e32 v0, 0x21000
	v_mad_u32_u24 v50, v13, s0, v0
	v_mov_b32_e32 v0, 0x26800
	v_mad_u32_u24 v52, v13, s0, v0
	v_lshlrev_b32_e32 v0, 1, v11
	v_lshl_add_u64 v[32:33], s[14:15], 0, v[0:1]
	s_mov_b64 s[0:1], 0x5d00000
	v_lshl_add_u64 v[32:33], v[32:33], 0, s[0:1]
	s_mov_b64 s[0:1], 0x5e00000
	v_lshlrev_b32_e32 v2, 2, v11
	v_lshlrev_b32_e32 v20, 3, v11
	v_lshl_add_u64 v[34:35], v[22:23], 0, s[0:1]
	s_movk_i32 s0, 0x9a0
	v_mov_b32_e32 v11, 0x13400
	v_mad_u32_u24 v56, v13, s0, v11
	v_mov_b32_e32 v11, 0x18100
	s_add_u32 s22, s22, 0x40000
	v_lshlrev_b32_e32 v42, 2, v144
	v_mad_u32_u24 v58, v13, s0, v11
	v_mov_b32_e32 v11, 0x1ce00
	s_addc_u32 s23, s23, 0
	v_mov_b32_e32 v43, v1
	v_mad_u32_u24 v60, v13, s0, v11
	v_mov_b32_e32 v11, 0x21b00
	v_lshl_add_u64 v[40:41], s[16:17], 0, v[42:43]
	s_add_u32 s16, s26, 0x400000
	v_or_b32_e32 v9, 8, v13
	v_or_b32_e32 v15, 16, v13
	v_mad_u32_u24 v62, v13, s0, v11
	v_lshlrev_b32_e32 v11, 3, v144
	s_addc_u32 s17, s27, 0
	v_lshlrev_b32_e32 v4, 10, v13
	v_lshlrev_b32_e32 v6, 10, v9
	v_lshlrev_b32_e32 v8, 10, v15
	v_or_b32_e32 v17, 24, v13
	v_mul_u32_u24_e32 v5, 0x84, v13
	v_lshlrev_b32_e32 v24, 6, v13
	v_lshlrev_b32_e32 v26, 6, v9
	v_lshlrev_b32_e32 v28, 6, v15
	v_mul_u32_u24_e32 v44, 0xb00, v13
	v_and_b32_e32 v9, 32, v42
	v_mul_u32_u24_e32 v0, 0x9a0, v13
	v_and_b32_e32 v64, 0x1c0, v11
	v_lshrrev_b32_e32 v13, 4, v144
	v_or_b32_e32 v31, 64, v144
	s_movk_i32 s0, 0x180
	v_mov_b32_e32 v15, 0x6000
	v_or_b32_e32 v21, 0x80, v144
	v_mov_b32_e32 v19, 0xc000
	v_or_b32_e32 v27, 0xc0, v144
	v_lshl_add_u64 v[42:43], s[20:21], 0, v[42:43]
	s_add_u32 s20, s6, 0x9a0000
	v_lshlrev_b32_e32 v10, 10, v17
	v_or_b32_e32 v12, 0x8000, v4
	v_or_b32_e32 v14, 0xa000, v4
	v_or_b32_e32 v16, 0xc000, v4
	v_or_b32_e32 v18, 0xe000, v4
	v_lshlrev_b32_e32 v30, 6, v17
	v_mul_u32_u24_e32 v11, 0x180, v144
	v_mad_u32_u24 v15, v144, s0, v15
	v_lshrrev_b32_e32 v17, 4, v31
	v_mad_u32_u24 v19, v144, s0, v19
	v_lshrrev_b32_e32 v21, 4, v21
	v_mad_u32_u24 v25, v144, s0, v226
	v_lshrrev_b32_e32 v27, 4, v27
	v_lshlrev_b32_e32 v36, 11, v144
	v_mov_b32_e32 v37, v1
	v_or_b32_e32 v29, 16, v13
	v_lshlrev_b32_e32 v38, 11, v31
	v_mov_b32_e32 v39, v1
	v_or_b32_e32 v31, 20, v13
	s_addc_u32 s21, s7, 0
	s_lshl_b32 s25, s2, 5
	s_lshl_b32 s26, s71, 5
	v_lshlrev_b32_e32 v44, 2, v44
	v_lshlrev_b32_e32 v46, 2, v46
	v_lshlrev_b32_e32 v48, 2, v48
	v_lshlrev_b32_e32 v50, 2, v50
	v_lshlrev_b32_e32 v52, 2, v52
	v_lshlrev_b32_e32 v54, 2, v0
	v_lshlrev_b32_e32 v56, 2, v56
	v_lshlrev_b32_e32 v58, 2, v58
	v_lshlrev_b32_e32 v60, 2, v60
	v_lshlrev_b32_e32 v62, 2, v62
	v_lshlrev_b32_e32 v64, 1, v64
	s_branch .LBB0_164

.LBB0_1104:
	s_waitcnt vmcnt(0)
	s_barrier
	s_cmp_lg_u32 s24, 0
	s_cbranch_scc1 .Lcv_g4_skip
	v_readlane_b32 s56, v251, 2
	s_nop 0
	s_sub_i32 s56, s56, 8
	s_lshl_b32 s56, s56, 3
	s_cmp_lt_i32 s56, 0
	s_cbranch_scc1 .Lcv_g4_skip
	s_sub_i32 s59, s70, 8
	s_lshl_b32 s59, s59, 3
	s_mov_b32 s57, 0x5dc0
	s_mov_b32 s58, 0xfa0
	s_mov_b32 s60, 0x6d60
	s_mov_b32 s61, 1
	s_mov_b32 s62, s9
	s_mov_b32 s63, s13
	s_mov_b32 s64, s24
	s_mov_b32 s65, s55
	s_mov_b32 s66, s54
	s_mov_b32 s67, s52
	s_mov_b32 s68, s53
	v_readlane_b32 s0, v251, 8
	v_readlane_b32 s1, v251, 9
	s_nop 0
	s_load_dwordx2 s[2:3], s[0:1], 0x40
	s_load_dwordx4 s[4:7], s[0:1], 0x60
	s_load_dwordx8 s[12:19], s[0:1], 0xd8
	s_load_dwordx2 s[20:21], s[0:1], 0xc8
	s_load_dwordx4 s[24:27], s[0:1], 0x78
	s_load_dwordx2 s[28:29], s[0:1], 0xf8
	v_mbcnt_lo_u32_b32 v75, -1, 0
	v_mbcnt_hi_u32_b32 v75, -1, v75
	v_readlane_b32 s30, v251, 4
	v_and_b32_e32 v74, 63, v75
	s_waitcnt lgkmcnt(0)
	v_writelane_b32 v253, s2, 19
	s_nop 1
	v_writelane_b32 v253, s3, 20
	s_nop 1
	v_writelane_b32 v253, s4, 21
	s_nop 1
	v_writelane_b32 v253, s5, 22
	s_nop 1
	v_writelane_b32 v253, s6, 23
	s_nop 1
	v_writelane_b32 v253, s7, 24
	s_nop 1
	v_writelane_b32 v253, s24, 25
	s_nop 1
	v_writelane_b32 v253, s25, 26
	s_nop 1
	v_writelane_b32 v253, s26, 27
	s_nop 1
	v_writelane_b32 v253, s27, 28
	s_nop 1
	v_writelane_b32 v253, s20, 29
	s_nop 1
	v_writelane_b32 v253, s21, 30
	s_nop 1
	v_writelane_b32 v253, s28, 31
	s_nop 1
	v_writelane_b32 v253, s29, 32
	s_nop 1
	v_writelane_b32 v253, s12, 33
	s_nop 1
	v_writelane_b32 v253, s13, 34
	s_nop 1
	v_writelane_b32 v253, s14, 35
	s_nop 1
	v_writelane_b32 v253, s15, 36
	s_nop 1
	v_writelane_b32 v253, s16, 37
	s_nop 1
	v_writelane_b32 v253, s17, 38
	s_nop 1
	v_writelane_b32 v253, s18, 39
	s_nop 1
	v_writelane_b32 v253, s19, 40
	s_nop 1
	v_add_u32_e32 v10, s30, v75
	s_nop 0
	v_readfirstlane_b32 s0, v10
	s_ashr_i32 s0, s0, 6
	s_nop 0
	v_writelane_b32 v253, s0, 41
	s_nop 1
	s_branch .Lcv_entry
